# S12: S10 + s_setprio 3 on the 4 adj-loader waves (the waves that issue the HBM stream)
# speedup vs baseline: 1.0017x; 1.0017x over previous
.LBB1_65:
	s_andn2_saveexec_b64 s[4:5], s[12:13]
	s_cbranch_execz .LBB1_103
	s_setprio 3
	s_load_dwordx2 s[4:5], s[0:1], 0x0
	s_load_dwordx2 s[6:7], s[0:1], 0x10
	v_mov_b32_e32 v128, v102
	v_readfirstlane_b32 s8, v98
	v_and_b32_e32 v129, 15, v128
	v_lshrrev_b32_e32 v130, 4, v128
	v_lshlrev_b32_e32 v138, 4, v128
	s_add_i32 s8, s8, -8
	s_add_i32 s10, s3, 26
	s_mov_b32 s12, 0x2aaaaaab
	s_mul_i32 s9, s28, 48
	s_sub_i32 s9, s3, s9
	v_lshrrev_b32_e32 v133, 2, v129
	v_and_b32_e32 v134, 1, v129
	v_bfe_u32 v135, v129, 1, 1
	v_lshl_or_b32 v134, v134, 1, v135
	v_lshlrev_b32_e32 v134, 3, v134
	v_lshl_or_b32 v134, v133, 5, v134
	s_mul_i32 s11, s8, 2304
	s_add_i32 s11, s11, 87040
	s_movk_i32 s13, 9216
	v_mad_u32_u24 v131, v130, s13, v134
	v_add_u32_e32 v131, s11, v131
	v_lshlrev_b32_e32 v129, 4, v129
	s_mul_hi_u32 s11, s28, s12
	s_lshr_b32 s11, s11, 3
	s_mul_i32 s17, s11, 48
	s_sub_i32 s17, s28, s17
	s_mov_b32 s16, s9
	s_mul_i32 s11, s11, 192
	s_lshl_b32 s13, s9, 2
	s_add_i32 s11, s11, s13
	s_lshl_b32 s11, s11, 8
	s_waitcnt lgkmcnt(0)
	s_add_u32 s14, s6, s11
	s_addc_u32 s15, s7, 0
	s_mul_i32 s11, s8, 0x30000
	s_add_u32 s64, s4, s11
	s_addc_u32 s65, s5, 0
	s_add_u32 s66, s64, 0x3000
	s_addc_u32 s67, s65, 0
	s_add_u32 s68, s66, 0x3000
	s_addc_u32 s69, s67, 0
	s_add_u32 s70, s68, 0x3000
	s_addc_u32 s71, s69, 0
	s_add_u32 s72, s70, 0x3000
	s_addc_u32 s73, s71, 0
	s_add_u32 s74, s72, 0x3000
	s_addc_u32 s75, s73, 0
	s_add_u32 s76, s74, 0x3000
	s_addc_u32 s77, s75, 0
	s_add_u32 s78, s76, 0x3000
	s_addc_u32 s79, s77, 0
	s_add_u32 s80, s78, 0x3000
	s_addc_u32 s81, s79, 0
	s_add_u32 s82, s80, 0x3000
	s_addc_u32 s83, s81, 0
	s_add_u32 s84, s82, 0x3000
	s_addc_u32 s85, s83, 0
	s_add_u32 s86, s84, 0x3000
	s_addc_u32 s87, s85, 0
	s_add_u32 s88, s86, 0x3000
	s_addc_u32 s89, s87, 0
	s_add_u32 s90, s88, 0x3000
	s_addc_u32 s91, s89, 0
	s_add_u32 s92, s90, 0x3000
	s_addc_u32 s93, s91, 0
	s_add_u32 s94, s92, 0x3000
	s_addc_u32 s95, s93, 0
	global_load_dwordx4 v[140:143], v138, s[14:15]
	s_add_u32 s14, s14, 0x400
	s_addc_u32 s15, s15, 0
	s_add_i32 s16, s16, 1
	s_cmp_lg_u32 s16, 48
	s_cbranch_scc1 .Lld_bbn0
	s_mov_b32 s16, 0
	s_add_i32 s17, s17, 1
	s_cmp_lg_u32 s17, 48
	s_cbranch_scc1 .Lld_bbw0
	s_mov_b32 s17, 0
	s_branch .Lld_bbn0
